# speedup vs baseline: 1.0279x; 1.0016x over previous
_Z15finalize_kernelPKfPKiPK15HIP_vector_typeIfLj2EES0_S2_S2_Pf:
	s_load_dwordx4 s[4:7], s[0:1], 0x0
	s_load_dwordx4 s[28:31], s[0:1], 0x18
	s_load_dwordx2 s[32:33], s[0:1], 0x28
	v_lshl_or_b32 v2, s2, 8, v0
	v_ashrrev_i32_e32 v3, 31, v2
	v_lshlrev_b64 v[4:5], 2, v[2:3]
	v_mov_b32_e32 v11, 0
	v_lshlrev_b32_e32 v19, 2, v2
	s_waitcnt lgkmcnt(0)
	v_lshl_add_u64 v[6:7], s[6:7], 0, v[4:5]
	global_load_dword v10, v[6:7], off
	v_lshl_add_u64 v[4:5], s[4:5], 0, v[4:5]
	global_load_dword v1, v[4:5], off
	global_load_dword v20, v19, s[30:31]
	global_load_dword v21, v19, s[28:29]
	s_load_dword s34, s[32:33], 0x0
	s_load_dwordx8 s[4:11], s[0:1], 0x18
	s_waitcnt vmcnt(1)
	v_cmp_lt_i32_e32 vcc, 0, v10
	s_and_saveexec_b64 s[12:13], vcc
	s_cbranch_execz .LBB2_12
	s_load_dwordx2 s[14:15], s[0:1], 0x10
	s_movk_i32 s0, 0x7d0
	v_mov_b32_e32 v4, 0xf149f2ca
	s_waitcnt vmcnt(0)
	v_cmp_lt_f32_e32 vcc, 0, v1
	v_mad_i64_i32 v[6:7], s[0:1], v2, s0, 0
	s_nop 0
	v_cndmask_b32_e64 v11, v4, 0, vcc
	s_mov_b32 s18, 1
	v_cmp_ne_u32_e64 s[0:1], 1, v10
	s_mov_b64 s[20:21], -1
	v_mov_b32_e32 v8, 0
	s_waitcnt lgkmcnt(0)
	v_lshl_add_u64 v[4:5], s[14:15], 0, v[6:7]
	s_and_saveexec_b64 s[16:17], s[0:1]
	s_cbranch_execz .LBB2_5
	s_mov_b32 s23, 0
	v_and_b32_e32 v9, 0x7ffffffe, v10
	s_mov_b32 s26, 2
	s_mov_b64 s[24:25], 0
	v_mov_b32_e32 v13, v11
	s_mov_b32 s22, s23

.LBB2_12:
	s_or_b64 exec, exec, s[12:13]
	s_waitcnt lgkmcnt(0)
	s_movk_i32 s0, 0xff9c
	s_waitcnt vmcnt(0)
	v_cmp_ne_u32_e32 vcc, s0, v20
	v_mov_b32_e32 v4, 0
	s_and_saveexec_b64 s[0:1], vcc
	s_cbranch_execz .LBB2_14
	s_mov_b32 s2, 0x800000
	v_cmp_gt_f32_e32 vcc, s2, v1
	v_mov_b32_e32 v3, 0x42000000
	s_mov_b32 s2, 0x3f317218
	v_cndmask_b32_e64 v4, 0, 32, vcc
	v_ldexp_f32 v1, v1, v4
	v_log_f32_e32 v1, v1
	v_cndmask_b32_e32 v3, 0, v3, vcc
	v_sub_f32_e32 v1, v1, v3
	v_add_f32_e32 v1, v11, v1
	v_fma_f32 v4, v1, s2, -v21

.LBB2_16:
	s_or_b64 exec, exec, s[0:1]
	v_cmp_eq_u32_e32 vcc, 0, v0
	s_waitcnt lgkmcnt(0)
	s_barrier
	s_and_saveexec_b64 s[0:1], vcc
	s_cbranch_execz .LBB2_19
	s_mov_b64 s[0:1], exec
	v_mbcnt_lo_u32_b32 v0, s0, 0
	v_mbcnt_hi_u32_b32 v0, s1, v0
	v_cmp_eq_u32_e32 vcc, 0, v0
	s_and_b64 s[2:3], exec, vcc
	s_mov_b64 exec, s[2:3]
	s_cbranch_execz .LBB2_19
	v_mov_b32_e32 v4, 0
	s_mov_b32 s2, s34
	ds_read_b128 v[0:3], v4
	s_bcnt1_i32_b64 s0, s[0:1]
	s_waitcnt lgkmcnt(0)
	v_cvt_f32_i32_e32 v5, s2
	v_add_f32_e32 v0, v0, v1
	v_add_f32_e32 v0, v0, v2
	v_add_f32_e32 v0, v0, v3
	v_div_scale_f32 v1, s[2:3], v5, v5, v0
	v_rcp_f32_e32 v2, v1
	v_div_scale_f32 v3, vcc, v0, v5, v0
	v_fma_f32 v6, -v1, v2, 1.0
	v_fmac_f32_e32 v2, v6, v2
	v_mul_f32_e32 v6, v3, v2
	v_fma_f32 v7, -v1, v6, v3
	v_fmac_f32_e32 v6, v7, v2
	v_fma_f32 v1, -v1, v6, v3
	v_div_fmas_f32 v1, v1, v2, v6
	v_div_fixup_f32 v0, v1, v5, v0
	v_cvt_f32_ubyte0_e32 v1, s0
	v_mul_f32_e32 v0, v0, v1
	global_atomic_add_f32 v4, v0, s[10:11]

	.amdhsa_kernel _Z15finalize_kernelPKfPKiPK15HIP_vector_typeIfLj2EES0_S2_S2_Pf
		.amdhsa_group_segment_fixed_size 16
		.amdhsa_private_segment_fixed_size 0
		.amdhsa_kernarg_size 56
		.amdhsa_user_sgpr_count 2
		.amdhsa_user_sgpr_dispatch_ptr 0
		.amdhsa_user_sgpr_queue_ptr 0
		.amdhsa_user_sgpr_kernarg_segment_ptr 1
		.amdhsa_user_sgpr_dispatch_id 0
		.amdhsa_user_sgpr_kernarg_preload_length 0
		.amdhsa_user_sgpr_kernarg_preload_offset 0
		.amdhsa_user_sgpr_private_segment_size 0
		.amdhsa_uses_dynamic_stack 0
		.amdhsa_enable_private_segment 0
		.amdhsa_system_sgpr_workgroup_id_x 1
		.amdhsa_system_sgpr_workgroup_id_y 0
		.amdhsa_system_sgpr_workgroup_id_z 0
		.amdhsa_system_sgpr_workgroup_info 0
		.amdhsa_system_vgpr_workitem_id 0
		.amdhsa_next_free_vgpr 24
		.amdhsa_next_free_sgpr 36
		.amdhsa_accum_offset 24
		.amdhsa_reserve_vcc 1
		.amdhsa_float_round_mode_32 0
		.amdhsa_float_round_mode_16_64 0
		.amdhsa_float_denorm_mode_32 3
		.amdhsa_float_denorm_mode_16_64 3
		.amdhsa_dx10_clamp 1
		.amdhsa_ieee_mode 1
		.amdhsa_fp16_overflow 0
		.amdhsa_tg_split 0
		.amdhsa_exception_fp_ieee_invalid_op 0
		.amdhsa_exception_fp_denorm_src 0
		.amdhsa_exception_fp_ieee_div_zero 0
		.amdhsa_exception_fp_ieee_overflow 0
		.amdhsa_exception_fp_ieee_underflow 0
		.amdhsa_exception_fp_ieee_inexact 0
		.amdhsa_exception_int_div_zero 0
	.end_amdhsa_kernel

amdhsa.kernels:
  - .agpr_count:     0
    .args:
      - .actual_access:  read_only
        .address_space:  global
        .offset:         0
        .size:           8
        .value_kind:     global_buffer
      - .actual_access:  read_only
        .address_space:  global
        .offset:         8
        .size:           8
        .value_kind:     global_buffer
      - .actual_access:  read_only
        .address_space:  global
        .offset:         16
        .size:           8
        .value_kind:     global_buffer
      - .actual_access:  write_only
        .address_space:  global
        .offset:         24
        .size:           8
        .value_kind:     global_buffer
      - .actual_access:  write_only
        .address_space:  global
        .offset:         32
        .size:           8
        .value_kind:     global_buffer
      - .actual_access:  write_only
        .address_space:  global
        .offset:         40
        .size:           8
        .value_kind:     global_buffer
      - .actual_access:  write_only
        .address_space:  global
        .offset:         48
        .size:           8
        .value_kind:     global_buffer
      - .actual_access:  write_only
        .address_space:  global
        .offset:         56
        .size:           8
        .value_kind:     global_buffer
      - .actual_access:  write_only
        .address_space:  global
        .offset:         64
        .size:           8
        .value_kind:     global_buffer
      - .actual_access:  write_only
        .address_space:  global
        .offset:         72
        .size:           8
        .value_kind:     global_buffer
      - .actual_access:  write_only
        .address_space:  global
        .offset:         80
        .size:           8
        .value_kind:     global_buffer
    .group_segment_fixed_size: 49152
    .kernarg_segment_align: 8
    .kernarg_segment_size: 88
    .language:       OpenCL C
    .language_version:
      - 2
      - 0
    .max_flat_workgroup_size: 256
    .name:           _Z12quant_kernelPKfS0_PKiPhS3_PjS4_PfS5_S5_Pi
    .private_segment_fixed_size: 0
    .sgpr_count:     31
    .sgpr_spill_count: 0
    .symbol:         _Z12quant_kernelPKfS0_PKiPhS3_PjS4_PfS5_S5_Pi.kd
    .uniform_work_group_size: 1
    .uses_dynamic_stack: false
    .vgpr_count:     163
    .vgpr_spill_count: 0
    .wavefront_size: 64
  - .agpr_count:     0
    .args:
      - .actual_access:  read_only
        .address_space:  global
        .offset:         0
        .size:           8
        .value_kind:     global_buffer
      - .actual_access:  read_only
        .address_space:  global
        .offset:         8
        .size:           8
        .value_kind:     global_buffer
      - .address_space:  global
        .offset:         16
        .size:           8
        .value_kind:     global_buffer
      - .address_space:  global
        .offset:         24
        .size:           8
        .value_kind:     global_buffer
      - .address_space:  global
        .offset:         32
        .size:           8
        .value_kind:     global_buffer
      - .address_space:  global
        .offset:         40
        .size:           8
        .value_kind:     global_buffer
      - .actual_access:  write_only
        .address_space:  global
        .offset:         48
        .size:           8
        .value_kind:     global_buffer
    .group_segment_fixed_size: 126976
    .kernarg_segment_align: 8
    .kernarg_segment_size: 56
    .language:       OpenCL C
    .language_version:
      - 2
      - 0
    .max_flat_workgroup_size: 512
    .name:           _Z15gemm_lse_kernelPKhS0_PKjS2_PfPiP15HIP_vector_typeIfLj2EE
    .private_segment_fixed_size: 0
    .sgpr_count:     48
    .sgpr_spill_count: 0
    .symbol:         _Z15gemm_lse_kernelPKhS0_PKjS2_PfPiP15HIP_vector_typeIfLj2EE.kd
    .uniform_work_group_size: 1
    .uses_dynamic_stack: false
    .vgpr_count:     256
    .vgpr_spill_count: 0
    .wavefront_size: 64
  - .agpr_count:     0
    .args:
      - .actual_access:  read_only
        .address_space:  global
        .offset:         0
        .size:           8
        .value_kind:     global_buffer
      - .actual_access:  read_only
        .address_space:  global
        .offset:         8
        .size:           8
        .value_kind:     global_buffer
      - .actual_access:  read_only
        .address_space:  global
        .offset:         16
        .size:           8
        .value_kind:     global_buffer
      - .actual_access:  read_only
        .address_space:  global
        .offset:         24
        .size:           8
        .value_kind:     global_buffer
      - .actual_access:  read_only
        .address_space:  global
        .offset:         32
        .size:           8
        .value_kind:     global_buffer
      - .actual_access:  read_only
        .address_space:  global
        .offset:         40
        .size:           8
        .value_kind:     global_buffer
      - .address_space:  global
        .offset:         48
        .size:           8
        .value_kind:     global_buffer
    .group_segment_fixed_size: 16
    .kernarg_segment_align: 8
    .kernarg_segment_size: 56
    .language:       OpenCL C
    .language_version:
      - 2
      - 0
    .max_flat_workgroup_size: 256
    .name:           _Z15finalize_kernelPKfPKiPK15HIP_vector_typeIfLj2EES0_S2_S2_Pf
    .private_segment_fixed_size: 0
    .sgpr_count:     33
    .sgpr_spill_count: 0
    .symbol:         _Z15finalize_kernelPKfPKiPK15HIP_vector_typeIfLj2EES0_S2_S2_Pf.kd
    .uniform_work_group_size: 1
    .uses_dynamic_stack: false
    .vgpr_count:     24
    .vgpr_spill_count: 0
    .wavefront_size: 64
